# v43
# baseline (speedup 1.0000x reference)
_Z3k_BPKiS0_PiS1_PKfPDF16_:
	v_cmp_eq_u32_e32 vcc, 0, v0
	s_and_saveexec_b64 s[4:5], vcc
	v_mov_b32_e32 v2, 0
	v_mov_b32_e32 v3, v2
	ds_write_b64 v2, v[2:3] offset:27712
	s_or_b64 exec, exec, s[4:5]
	s_load_dwordx2 s[24:25], s[0:1], 0x0
	s_load_dwordx4 s[36:39], s[0:1], 0x20
	s_movk_i32 s3, 0x100
	v_cmp_gt_u32_e32 vcc, s3, v0
	v_mbcnt_lo_u32_b32 v16, -1, 0
	v_and_b32_e32 v14, 63, v0
	s_waitcnt lgkmcnt(0)
	s_lshl_b32 s40, s2, 10
	s_add_i32 s40, s40, 0x124f80
	v_add_u32_e32 v60, s40, v0
	v_min_u32_e32 v61, 0x1869ff, v60
	v_lshlrev_b32_e32 v61, 5, v61
	global_load_dwordx4 v[28:31], v61, s[36:37]
	global_load_dwordx4 v[32:35], v61, s[36:37] offset:16
	s_barrier
	s_and_saveexec_b64 s[6:7], vcc
	s_cbranch_execz .LBB1_12
	s_load_dwordx2 s[4:5], s[0:1], 0x8
	s_lshl_b32 s3, s2, 8
	v_or_b32_e32 v2, s3, v0
	s_addk_i32 s3, 0x100
	v_ashrrev_i32_e32 v3, 31, v2
	v_or_b32_e32 v4, s3, v0
	s_waitcnt lgkmcnt(0)
	v_lshl_add_u64 v[2:3], v[2:3], 2, s[4:5]
	v_ashrrev_i32_e32 v5, 31, v4
	v_lshl_add_u64 v[4:5], v[4:5], 2, s[4:5]
	global_load_dword v1, v[2:3], off
	global_load_dword v6, v[4:5], off
	v_mbcnt_hi_u32_b32 v2, -1, v16
	v_and_b32_e32 v3, 64, v2
	v_xor_b32_e32 v4, 32, v2
	v_add_u32_e32 v3, 64, v3
	v_cmp_lt_i32_e64 s[4:5], v4, v3
	v_xor_b32_e32 v7, 16, v2
	v_xor_b32_e32 v8, 8, v2
	v_cndmask_b32_e64 v4, v2, v4, s[4:5]
	v_lshlrev_b32_e32 v4, 2, v4
	v_cmp_lt_i32_e64 s[4:5], v7, v3
	v_xor_b32_e32 v9, 4, v2
	v_xor_b32_e32 v10, 2, v2
	v_cndmask_b32_e64 v7, v2, v7, s[4:5]
	v_lshlrev_b32_e32 v7, 2, v7
	v_cmp_lt_i32_e64 s[4:5], v8, v3
	v_xor_b32_e32 v11, 1, v2
	s_movk_i32 s3, 0x1870
	v_cndmask_b32_e64 v8, v2, v8, s[4:5]
	v_lshlrev_b32_e32 v8, 2, v8
	v_cmp_lt_i32_e64 s[4:5], v9, v3
	v_lshlrev_b32_e32 v5, 2, v0
	s_waitcnt vmcnt(1)
	ds_bpermute_b32 v12, v4, v1
	s_waitcnt vmcnt(0)
	v_sub_u32_e32 v6, v6, v1
	ds_bpermute_b32 v4, v4, v6
	v_cndmask_b32_e64 v9, v2, v9, s[4:5]
	v_lshlrev_b32_e32 v9, 2, v9
	s_waitcnt lgkmcnt(1)
	v_add_u32_e32 v12, v12, v1
	ds_bpermute_b32 v13, v7, v12
	s_waitcnt lgkmcnt(1)
	v_add_u32_e32 v4, v4, v6
	ds_bpermute_b32 v7, v7, v4
	v_cmp_lt_i32_e64 s[4:5], v10, v3
	s_waitcnt lgkmcnt(1)
	v_add_u32_e32 v12, v13, v12
	v_cndmask_b32_e64 v10, v2, v10, s[4:5]
	s_waitcnt lgkmcnt(0)
	v_add_u32_e32 v4, v7, v4
	ds_bpermute_b32 v7, v8, v12
	ds_bpermute_b32 v8, v8, v4
	v_lshlrev_b32_e32 v10, 2, v10
	v_cmp_lt_i32_e64 s[4:5], v11, v3
	s_waitcnt lgkmcnt(1)
	v_add_u32_e32 v7, v7, v12
	s_waitcnt lgkmcnt(0)
	v_add_u32_e32 v4, v8, v4
	ds_bpermute_b32 v8, v9, v7
	ds_bpermute_b32 v9, v9, v4
	v_cndmask_b32_e64 v2, v2, v11, s[4:5]
	v_lshlrev_b32_e32 v2, 2, v2
	v_cmp_eq_u32_e64 s[4:5], 0, v14
	s_waitcnt lgkmcnt(1)
	v_add_u32_e32 v7, v8, v7
	s_waitcnt lgkmcnt(0)
	v_add_u32_e32 v4, v9, v4
	ds_bpermute_b32 v8, v10, v7
	ds_bpermute_b32 v9, v10, v4
	v_mad_u32_u24 v10, v0, s3, v1
	ds_write2st64_b32 v5, v6, v10 offset0:96 offset1:100
	v_mov_b32_e32 v6, 0
	s_waitcnt lgkmcnt(2)
	v_add_u32_e32 v3, v8, v7
	s_waitcnt lgkmcnt(1)
	v_add_u32_e32 v1, v9, v4
	ds_bpermute_b32 v4, v2, v3
	ds_bpermute_b32 v2, v2, v1
	ds_write_b32 v5, v6 offset:26624
	s_and_b64 exec, exec, s[4:5]
	s_cbranch_execz .LBB1_12
	s_mov_b64 s[4:5], exec
	s_waitcnt lgkmcnt(2)
	v_add_u32_e32 v3, v4, v3
	s_mov_b32 s8, 0
